# speedup vs baseline: 1.0157x; 1.0157x over previous
_Z11knrm_kernelPKfS0_PKiS2_S0_Pf:
	s_load_dwordx8 s[4:11], s[0:1], 0x0
	s_load_dwordx4 s[12:15], s[0:1], 0x20
	v_lshrrev_b32_e32 v1, 6, v0
	v_and_b32_e32 v120, 63, v0
	v_lshrrev_b32_e32 v100, 4, v0
	v_and_b32_e32 v123, 15, v0
	v_lshlrev_b32_e32 v124, 5, v1
	s_lshl_b32 s3, s2, 5
	v_lshl_or_b32 v8, s2, 8, v124
	v_or_b32_e32 v2, s3, v100
	s_movk_i32 s3, 0x4b0
	v_mul_lo_u32 v2, v2, s3
	v_mul_lo_u32 v99, v8, s3
	v_lshlrev_b32_e32 v132, 4, v120
	v_min_u32_e32 v193, 23, v120
	v_lshl_add_u32 v3, v123, 4, v2
	v_min_u32_e32 v4, 10, v123
	v_add_u32_e32 v192, v99, v132
	v_lshlrev_b32_e32 v193, 4, v193
	s_movk_i32 s27, 0x1000
	s_movk_i32 s28, 0x2000
	v_lshl_add_u32 v2, v4, 4, v2
	v_add3_u32 v193, v99, v193, s28
	s_mov_b32 s19, 0x20000
	s_mov_b32 s18, 0x4b00000
	s_waitcnt lgkmcnt(0)
	s_mov_b64 s[16:17], s[6:7]
	s_and_b32 s5, s5, 0xffff
	s_mov_b32 s6, 0x960000
	s_mov_b32 s7, s19
	s_and_b32 s17, s17, 0xffff
	buffer_load_dwordx4 v[90:93], v3, s[4:7], 0 offen nt
	buffer_load_dwordx4 v[86:89], v3, s[4:7], 0 offen offset:256 nt
	buffer_load_dwordx4 v[82:85], v3, s[4:7], 0 offen offset:512 nt
	buffer_load_dwordx4 v[78:81], v3, s[4:7], 0 offen offset:768 nt
	buffer_load_dwordx4 v[94:97], v2, s[4:7], 0 offen offset:1024 nt
	buffer_load_dwordx4 v[2:5], v192, s[16:19], 0 offen nt
	buffer_load_dwordx4 v[14:17], v192, s[16:19], 0 offen offset:1024 nt
	buffer_load_dwordx4 v[34:37], v192, s[16:19], 0 offen offset:2048 nt
	buffer_load_dwordx4 v[46:49], v192, s[16:19], 0 offen offset:3072 nt
	buffer_load_dwordx4 v[54:57], v192, s[16:19], s27 offen nt
	buffer_load_dwordx4 v[58:61], v192, s[16:19], s27 offen offset:1024 nt
	buffer_load_dwordx4 v[62:65], v192, s[16:19], s27 offen offset:2048 nt
	buffer_load_dwordx4 v[66:69], v192, s[16:19], s27 offen offset:3072 nt
	buffer_load_dwordx4 v[70:73], v192, s[16:19], s28 offen nt
	buffer_load_dwordx4 v[74:77], v193, s[16:19], 0 offen offset:1024 nt
	v_lshlrev_b32_e32 v42, 2, v0
	v_bfe_u32 v43, v0, 2, 2
	v_and_or_b32 v98, v42, 12, v43
	v_and_or_b32 v6, v98, 7, v8
	v_ashrrev_i32_e32 v7, 31, v6
	s_movk_i32 s0, 0x160
	v_lshl_add_u64 v[6:7], v[6:7], 2, s[10:11]
	v_lshrrev_b32_e32 v121, 5, v0
	v_cmp_gt_u32_e64 s[0:1], s0, v0
	global_load_dword v125, v[6:7], off
	global_load_dword v126, v[6:7], off offset:64
	global_load_dword v127, v[6:7], off offset:96
	global_load_dword v190, v[6:7], off offset:32
	v_cndmask_b32_e64 v42, 10, v121, s[0:1]
	v_lshlrev_b32_e32 v42, 2, v42
	s_lshl_b32 s3, s2, 5
	v_and_b32_e32 v122, 31, v0
	global_load_dword v118, v42, s[12:13]
	v_or_b32_e32 v42, s3, v122
	v_ashrrev_i32_e32 v43, 31, v42
	v_lshl_add_u64 v[42:43], v[42:43], 2, s[8:9]
	global_load_dword v119, v[42:43], off
	s_mov_b32 s3, 0
	v_mul_u32_u24_e32 v131, 0x2600, v1
	v_cmp_gt_u32_e64 s[4:5], 16, v120
	s_and_saveexec_b64 s[6:7], s[4:5]
	s_movk_i32 s8, 0x260
	v_mov_b32_e32 v102, 0
	v_mad_u32_u24 v101, v120, s8, v131
	v_mov_b32_e32 v103, v102
	ds_write_b64 v101, v[102:103] offset:20056
	s_or_b64 exec, exec, s[6:7]
	v_cmp_lt_u32_e32 vcc, 10, v123
	s_waitcnt vmcnt(19)
	v_mul_f32_e32 v101, v87, v87
	v_mov_b32_e32 v106, v92
	s_waitcnt vmcnt(16)
	v_cndmask_b32_e64 v103, v97, 0, vcc
	v_cndmask_b32_e64 v102, v96, 0, vcc
	v_mov_b32_e32 v96, v91
	v_mov_b32_e32 v97, v83
	v_cndmask_b32_e64 v105, v95, 0, vcc
	v_cndmask_b32_e64 v104, v94, 0, vcc
	v_mov_b32_e32 v94, v90
	v_mov_b32_e32 v95, v82
	v_pk_mul_f32 v[96:97], v[96:97], v[96:97]
	v_mov_b32_e32 v107, v84
	v_fmac_f32_e32 v101, v86, v86
	v_pk_fma_f32 v[94:95], v[94:95], v[94:95], v[96:97]
	v_mov_b32_e32 v108, v93
	v_mov_b32_e32 v109, v85
	v_fmac_f32_e32 v101, v88, v88
	v_pk_fma_f32 v[94:95], v[106:107], v[106:107], v[94:95]
	v_fmac_f32_e32 v101, v89, v89
	v_pk_fma_f32 v[94:95], v[108:109], v[108:109], v[94:95]
	v_mov_b32_e32 v96, v79
	v_add_f32_e32 v94, v94, v101
	v_mov_b32_e32 v97, v105
	v_add_f32_e32 v101, v94, v95
	v_mov_b32_e32 v94, v78
	v_mov_b32_e32 v95, v104
	v_pk_mul_f32 v[96:97], v[96:97], v[96:97]
	s_mov_b32 s21, 0xf800000
	v_pk_fma_f32 v[94:95], v[94:95], v[94:95], v[96:97]
	v_mov_b32_e32 v96, v80
	v_mov_b32_e32 v97, v102
	v_pk_fma_f32 v[94:95], v[96:97], v[96:97], v[94:95]
	v_mov_b32_e32 v96, v81
	v_mov_b32_e32 v97, v103
	v_pk_fma_f32 v[94:95], v[96:97], v[96:97], v[94:95]
	v_mov_b32_e32 v135, 0x260
	v_add_f32_e32 v94, v101, v94
	v_add_f32_e32 v94, v94, v95
	v_mbcnt_lo_u32_b32 v95, -1, 0
	v_mbcnt_hi_u32_b32 v95, -1, v95
	v_and_b32_e32 v97, 64, v95
	v_add_u32_e32 v101, 64, v97
	s_movk_i32 s8, 0x260
	v_add_u32_e32 v137, 0x4b00, v99
	s_movk_i32 s10, 0x1b5
	v_mov_b32_e32 v99, 0x36a00
	v_mov_b32_e32 v111, 0x666c0
	v_mov_b32_e32 v113, 0x6d400
	v_mov_b32_e32 v115, 0x74140
	s_mov_b32 s20, 0xbeb17218
	s_mov_b32 s22, 0x44132d1f
	v_mov_b32_e32 v161, 0xc47a0000
	v_add_f32_dpp v96, v94, v94 quad_perm:[1,0,3,2] row_mask:0xf bank_mask:0xf
	s_nop 1
	v_add_f32_dpp v94, v96, v96 quad_perm:[2,3,0,1] row_mask:0xf bank_mask:0xf
	s_nop 1
	v_add_f32_dpp v96, v94, v94 row_half_mirror row_mask:0xf bank_mask:0xf
	s_nop 1
	v_add_f32_dpp v94, v96, v96 row_mirror row_mask:0xf bank_mask:0xf
	v_mul_f32_e32 v96, 0x4f800000, v94
	v_cmp_gt_f32_e32 vcc, s21, v94
	s_nop 1
	v_cndmask_b32_e32 v94, v94, v96, vcc
	v_sqrt_f32_e32 v96, v94
	s_nop 0
	v_add_u32_e32 v106, -1, v96
	v_fma_f32 v107, -v106, v96, v94
	v_cmp_ge_f32_e64 s[6:7], 0, v107
	v_add_u32_e32 v107, 1, v96
	s_nop 0
	v_cndmask_b32_e64 v106, v96, v106, s[6:7]
	v_fma_f32 v96, -v107, v96, v94
	v_cmp_lt_f32_e64 s[6:7], 0, v96
	s_nop 1
	v_cndmask_b32_e64 v96, v106, v107, s[6:7]
	v_mul_f32_e32 v106, 0x37800000, v96
	v_cndmask_b32_e32 v96, v96, v106, vcc
	v_cmp_class_f32_e32 vcc, v94, v135
	s_nop 1
	v_cndmask_b32_e32 v94, v96, v94, vcc
	v_add_f32_e32 v96, 0x29e12e13, v94
	v_div_scale_f32 v106, s[6:7], v96, v96, 1.0
	v_rcp_f32_e32 v107, v106
	v_mov_b32_e32 v94, 0
	v_cmp_gt_u32_e64 s[6:7], 48, v120
	v_mov_b32_e32 v116, v94
	v_fma_f32 v108, -v106, v107, 1.0
	v_fmac_f32_e32 v107, v108, v107
	v_div_scale_f32 v108, vcc, 1.0, v96, 1.0
	v_mul_f32_e32 v109, v108, v107
	v_fma_f32 v110, -v106, v109, v108
	v_fmac_f32_e32 v109, v110, v107
	v_fma_f32 v106, -v106, v109, v108
	v_div_fmas_f32 v106, v106, v107, v109
	v_div_fixup_f32 v96, v106, v96, 1.0
	v_lshlrev_b32_e32 v106, 3, v123
	v_pk_mul_f32 v[82:83], v[96:97], v[82:83] op_sel_hi:[0,1]
	v_pk_mul_f32 v[84:85], v[96:97], v[84:85] op_sel_hi:[0,1]
	v_pk_mul_f32 v[78:79], v[96:97], v[78:79] op_sel_hi:[0,1]
	v_pk_mul_f32 v[80:81], v[96:97], v[80:81] op_sel_hi:[0,1]
	v_mad_u32_u24 v100, v100, s8, v106
	v_cvt_pk_f16_f32 v82, v82, v83
	v_cvt_pk_f16_f32 v83, v84, v85
	v_cvt_pk_f16_f32 v78, v78, v79
	v_cvt_pk_f16_f32 v79, v80, v81
	ds_write2_b64 v100, v[82:83], v[78:79] offset0:32 offset1:48
	v_min_u32_e32 v82, 23, v120
	v_mov_b32_e32 v83, 0x2400
	v_lshl_or_b32 v138, v82, 4, v83
	v_xor_b32_e32 v83, 16, v95
	v_cmp_lt_i32_e32 vcc, v83, v101
	v_pk_mul_f32 v[90:91], v[96:97], v[90:91] op_sel_hi:[0,1]
	v_pk_mul_f32 v[92:93], v[96:97], v[92:93] op_sel_hi:[0,1]
	v_cndmask_b32_e32 v83, v95, v83, vcc
	v_lshlrev_b32_e32 v133, 2, v83
	v_xor_b32_e32 v83, 32, v95
	v_pk_mul_f32 v[86:87], v[96:97], v[86:87] op_sel_hi:[0,1]
	v_pk_mul_f32 v[88:89], v[96:97], v[88:89] op_sel_hi:[0,1]
	v_pk_mul_f32 v[78:79], v[96:97], v[104:105] op_sel_hi:[0,1]
	v_pk_mul_f32 v[80:81], v[96:97], v[102:103] op_sel_hi:[0,1]
	v_cmp_lt_i32_e32 vcc, v83, v101
	v_cvt_pk_f16_f32 v90, v90, v91
	v_cvt_pk_f16_f32 v91, v92, v93
	v_cvt_pk_f16_f32 v86, v86, v87
	v_cvt_pk_f16_f32 v87, v88, v89
	v_cvt_pk_f16_f32 v78, v78, v79
	v_cvt_pk_f16_f32 v79, v80, v81
	v_mov_b32_e32 v81, 0x17c00
	v_cndmask_b32_e32 v83, v95, v83, vcc
	ds_write2_b64 v100, v[90:91], v[86:87] offset1:16
	v_sub_u32_e64 v80, v123, 11 clamp
	v_lshl_or_b32 v81, v1, 7, v81
	v_lshlrev_b32_e32 v134, 2, v83
	v_or_b32_e32 v83, 64, v120
	v_mov_b32_e32 v86, 0x6d40
	v_mov_b32_e32 v87, 0xda80
	v_mov_b32_e32 v89, 0x147c0
	v_mov_b32_e32 v91, 0x1b500
	v_mov_b32_e32 v93, 0x28f80
	v_mov_b32_e32 v96, 0x2fcc0
	v_mov_b32_e32 v101, 0x3d740
	v_mov_b32_e32 v103, 0x44480
	v_mov_b32_e32 v105, 0x4b1c0
	v_mov_b32_e32 v107, 0x58c40
	v_or_b32_e32 v109, 0x3c0, v0
	v_mad_i32_i24 v80, v80, -8, v100
	v_lshrrev_b32_e32 v82, 1, v120
	v_lshl_add_u32 v139, v120, 2, v81
	v_and_or_b32 v140, v120, 48, v81
	v_lshlrev_b32_e32 v81, 3, v120
	v_mul_u32_u24_e32 v84, 0x1b5, v83
	v_lshl_add_u32 v85, v83, 3, v131
	v_mad_u32_u24 v86, v83, s10, v86
	v_mad_u32_u24 v87, v83, s10, v87
	v_mad_u32_u24 v89, v83, s10, v89
	v_mad_u32_u24 v91, v83, s10, v91
	v_mad_u32_u24 v93, v83, s10, v93
	v_mad_u32_u24 v96, v83, s10, v96
	v_mad_u32_u24 v99, v83, s10, v99
	v_mad_u32_u24 v101, v83, s10, v101
	v_mad_u32_u24 v103, v83, s10, v103
	v_mad_u32_u24 v105, v83, s10, v105
	v_mad_u32_u24 v107, v83, s10, v107
	v_mul_u32_u24_e32 v110, 0x1b5, v109
	v_mad_u32_u24 v111, v83, s10, v111
	v_mad_u32_u24 v113, v83, s10, v113
	v_mad_u32_u24 v83, v83, s10, v115
	ds_write_b64 v80, v[78:79] offset:512
	v_mul_u32_u24_e32 v78, 0x260, v123
	v_and_b32_e32 v82, 24, v82
	v_lshrrev_b32_e32 v84, 12, v84
	v_add_u32_e32 v141, v131, v81
	v_lshrrev_b32_e32 v86, 12, v86
	v_lshrrev_b32_e32 v87, 12, v87
	v_lshrrev_b32_e32 v89, 12, v89
	v_lshrrev_b32_e32 v91, 12, v91
	v_lshrrev_b32_e32 v93, 12, v93
	v_lshrrev_b32_e32 v96, 12, v96
	v_lshrrev_b32_e32 v99, 12, v99
	v_lshrrev_b32_e32 v101, 12, v101
	v_lshrrev_b32_e32 v103, 12, v103
	v_lshrrev_b32_e32 v105, 12, v105
	v_lshrrev_b32_e32 v107, 12, v107
	v_lshrrev_b32_e32 v110, 12, v110
	v_lshrrev_b32_e32 v111, 12, v111
	v_lshrrev_b32_e32 v113, 12, v113
	v_lshrrev_b32_e32 v83, 12, v83
	v_and_b32_e32 v79, 48, v0
	v_mad_u32_u24 v80, v98, s8, v131
	v_and_b32_e32 v84, 8, v84
	v_add_u32_e32 v81, 0x400, v141
	v_and_b32_e32 v86, 24, v86
	v_add_u32_e32 v88, 0x600, v141
	v_and_b32_e32 v87, 24, v87
	v_add_u32_e32 v90, 0x800, v141
	v_and_b32_e32 v89, 56, v89
	v_add_u32_e32 v92, 0xa00, v141
	v_and_b32_e32 v91, 56, v91
	v_add_u32_e32 v95, 0xe00, v141
	v_and_b32_e32 v93, 56, v93
	v_add_u32_e32 v98, 0x1000, v141
	v_and_b32_e32 v96, 56, v96
	v_add_u32_e32 v100, 0x1200, v141
	v_and_b32_e32 v99, 0x78, v99
	v_add_u32_e32 v102, 0x1400, v141
	v_and_b32_e32 v101, 0x78, v101
	v_add_u32_e32 v104, 0x1600, v141
	v_and_b32_e32 v103, 0x58, v103
	v_add_u32_e32 v106, 0x1800, v141
	v_and_b32_e32 v105, 0x58, v105
	v_add_u32_e32 v108, 0x1c00, v141
	v_and_b32_e32 v107, 0x78, v107
	v_lshl_add_u32 v109, v109, 3, v131
	v_and_b32_e32 v110, 0x78, v110
	v_add_u32_e32 v112, 0x2000, v141
	v_and_b32_e32 v111, 0x78, v111
	v_add_u32_e32 v114, 0x2200, v141
	v_and_b32_e32 v113, 0x78, v113
	v_add_u32_e32 v115, 0x2400, v141
	v_and_b32_e32 v83, 0xf8, v83
	s_movk_i32 s10, 0x4c00
	v_add_u32_e32 v78, v78, v82
	v_mad_u32_u24 v136, v123, s8, v79
	v_cmp_gt_u32_e64 s[8:9], 24, v120
	v_add3_u32 v142, v80, v79, s10
	v_add_u32_e32 v143, v85, v84
	v_add_u32_e32 v144, v81, v86
	v_add_u32_e32 v145, v88, v87
	v_add_u32_e32 v146, v90, v89
	v_add_u32_e32 v147, v92, v91
	v_add_u32_e32 v148, v95, v93
	v_add_u32_e32 v149, v98, v96
	v_add_u32_e32 v150, v100, v99
	v_add_u32_e32 v151, v102, v101
	v_add_u32_e32 v152, v104, v103
	v_add_u32_e32 v153, v106, v105
	v_add_u32_e32 v154, v108, v107
	v_add_u32_e32 v155, v109, v110
	v_add_u32_e32 v156, v112, v111
	v_add_u32_e32 v157, v114, v113
	v_add_u32_e32 v158, v115, v83
	v_add_u32_e32 v159, v80, v82
	v_add_u32_e32 v160, 64, v78
	v_mov_b32_e32 v96, 0xc604b4df
	v_mov_b32_e32 v95, v94
	v_mov_b32_e32 v98, v94
	v_mov_b32_e32 v99, v94
	v_mov_b32_e32 v100, v94
	v_mov_b32_e32 v101, v94
	v_mov_b32_e32 v102, v94
	v_mov_b32_e32 v103, v94
	v_mov_b32_e32 v104, v94
	v_mov_b32_e32 v105, v94
	v_mov_b32_e32 v106, v94
	v_mov_b32_e32 v107, v94
	v_mov_b32_e32 v108, v94
	v_mov_b32_e32 v109, v94
	v_mov_b32_e32 v110, v94
	v_mov_b32_e32 v111, v94
	v_mov_b32_e32 v112, v94
	v_mov_b32_e32 v113, v94
	v_mov_b32_e32 v114, v94
	v_mov_b32_e32 v115, v94
	v_mov_b32_e32 v117, v94
	v_mov_b32_e32 v242, 0x18000
	ds_write_b32 v242, v94 offset:32
	s_waitcnt lgkmcnt(0)
	s_barrier
	s_mov_b32 s26, 0x2580
	s_mov_b32 s27, 0x3580
	s_mov_b32 s28, 0x4580
	buffer_load_dwordx4 v[6:9], v192, s[16:19], s26 offen nt
	buffer_load_dwordx4 v[10:13], v192, s[16:19], s26 offen offset:1024 nt
	buffer_load_dwordx4 v[18:21], v192, s[16:19], s26 offen offset:2048 nt
	buffer_load_dwordx4 v[22:25], v192, s[16:19], s26 offen offset:3072 nt
	buffer_load_dwordx4 v[26:29], v192, s[16:19], s27 offen nt
	buffer_load_dwordx4 v[30:33], v192, s[16:19], s27 offen offset:1024 nt
	buffer_load_dwordx4 v[38:41], v192, s[16:19], s27 offen offset:2048 nt
	buffer_load_dwordx4 v[42:45], v192, s[16:19], s27 offen offset:3072 nt
	buffer_load_dwordx4 v[50:53], v192, s[16:19], s28 offen nt
	buffer_load_dwordx4 v[186:189], v193, s[16:19], s26 offen offset:1024 nt
	s_waitcnt vmcnt(25)
	v_cvt_pk_f16_f32 v79, v4, v5
	v_cvt_pk_f16_f32 v78, v2, v3
	ds_write_b64 v141, v[78:79] offset:19456
	s_waitcnt vmcnt(24)
	v_cvt_pk_f16_f32 v79, v16, v17
	v_cvt_pk_f16_f32 v78, v14, v15
	ds_write_b64 v143, v[78:79] offset:19456
	s_waitcnt vmcnt(23)
	v_cvt_pk_f16_f32 v79, v36, v37
	v_cvt_pk_f16_f32 v78, v34, v35
	ds_write_b64 v144, v[78:79] offset:19456
	s_waitcnt vmcnt(22)
	v_cvt_pk_f16_f32 v79, v48, v49
	v_cvt_pk_f16_f32 v78, v46, v47
	ds_write_b64 v145, v[78:79] offset:19456
	s_waitcnt vmcnt(21)
	v_cvt_pk_f16_f32 v79, v56, v57
	v_cvt_pk_f16_f32 v78, v54, v55
	ds_write_b64 v146, v[78:79] offset:19456
	s_waitcnt vmcnt(20)
	v_cvt_pk_f16_f32 v79, v60, v61
	v_cvt_pk_f16_f32 v78, v58, v59
	ds_write_b64 v147, v[78:79] offset:19456
	s_waitcnt vmcnt(19)
	v_cvt_pk_f16_f32 v79, v64, v65
	v_cvt_pk_f16_f32 v78, v62, v63
	ds_write_b64 v141, v[78:79] offset:22568
	s_waitcnt vmcnt(18)
	v_cvt_pk_f16_f32 v79, v68, v69
	v_cvt_pk_f16_f32 v78, v66, v67
	ds_write_b64 v148, v[78:79] offset:19456
	s_waitcnt vmcnt(17)
	v_cvt_pk_f16_f32 v79, v72, v73
	v_cvt_pk_f16_f32 v78, v70, v71
	ds_write_b64 v149, v[78:79] offset:19456
	s_waitcnt vmcnt(16)
	v_cvt_pk_f16_f32 v79, v76, v77
	v_cvt_pk_f16_f32 v78, v74, v75
	s_and_saveexec_b64 s[12:13], s[8:9]
	ds_write_b64 v150, v[78:79] offset:19456
	s_or_b64 exec, exec, s[12:13]
	s_waitcnt vmcnt(10)
	v_cmp_lt_i32_e64 s[30:31], 1, v125
	v_cmp_lt_i32_e64 s[32:33], 1, v190
	v_cmp_lt_i32_e64 s[34:35], 1, v126
	v_cmp_lt_i32_e64 s[36:37], 1, v127
	v_cndmask_b32_e64 v191, 0, 1, s[30:31]
	v_cndmask_b32_e64 v190, 0, 2, s[32:33]
	v_cndmask_b32_e64 v126, 0, 4, s[34:35]
	v_cndmask_b32_e64 v127, 0, 8, s[36:37]
	v_or3_b32 v191, v191, v190, v126
	v_or_b32_e32 v191, v191, v127
	s_mov_b32 s26, 0x4b00
	s_mov_b32 s27, 0x5b00
	s_mov_b32 s28, 0x6b00
	buffer_load_dwordx4 v[2:5], v192, s[16:19], s26 offen nt
	buffer_load_dwordx4 v[14:17], v192, s[16:19], s26 offen offset:1024 nt
	buffer_load_dwordx4 v[34:37], v192, s[16:19], s26 offen offset:2048 nt
	buffer_load_dwordx4 v[46:49], v192, s[16:19], s26 offen offset:3072 nt
	buffer_load_dwordx4 v[54:57], v192, s[16:19], s27 offen nt
	buffer_load_dwordx4 v[58:61], v192, s[16:19], s27 offen offset:1024 nt
	buffer_load_dwordx4 v[62:65], v192, s[16:19], s27 offen offset:2048 nt
	buffer_load_dwordx4 v[66:69], v192, s[16:19], s27 offen offset:3072 nt
	buffer_load_dwordx4 v[70:73], v192, s[16:19], s28 offen nt
	buffer_load_dwordx4 v[74:77], v193, s[16:19], s26 offen offset:1024 nt
	s_mov_b32 s3, 0
	s_branch .LBB0_7

.LBB0_22:
	s_or_b64 exec, exec, s[4:5]
	v_cmp_eq_u32_e32 vcc, 0, v120
	s_nop 4
	v_add_f32_dpp v2, v3, v3 quad_perm:[1,0,3,2] row_mask:0xf bank_mask:0xf
	s_nop 1
	v_add_f32_dpp v3, v2, v2 quad_perm:[2,3,0,1] row_mask:0xf bank_mask:0xf
	s_nop 1
	v_add_f32_dpp v2, v3, v3 row_ror:4 row_mask:0xf bank_mask:0xf
	s_nop 1
	v_add_f32_dpp v3, v2, v2 row_ror:8 row_mask:0xf bank_mask:0xf
	s_nop 0
	v_mov_b32_e32 v2, v3
	s_nop 1
	v_permlane16_swap_b32_e32 v2, v3
	v_add_f32_e32 v3, v2, v3
	v_mov_b32_e32 v2, v3
	s_nop 1
	v_permlane32_swap_b32_e32 v2, v3
	v_add_f32_e32 v2, v2, v3
	s_and_saveexec_b64 s[0:1], vcc
	s_cbranch_execz .LBB0_26
	v_mov_b32_e32 v3, 0x18000
	v_lshl_or_b32 v1, v1, 2, v3
	v_mov_b32_e32 v4, 1
	ds_write_b32 v1, v2
	ds_add_rtn_u32 v4, v3, v4 offset:32
	s_ashr_i32 s3, s2, 31
	s_lshl_b64 s[0:1], s[2:3], 2
	s_add_u32 s0, s14, s0
	s_addc_u32 s1, s15, s1
	s_waitcnt lgkmcnt(0)
	v_cmp_eq_u32_e32 vcc, 7, v4
	s_and_b64 exec, exec, vcc
	s_cbranch_execz .LBB0_26
	ds_read_b128 v[4:7], v3 offset:16
	ds_read_b128 v[0:3], v3
	s_waitcnt lgkmcnt(0)
	v_add_f32_e32 v0, v0, v1
	v_add_f32_e32 v2, v2, v3
	v_add_f32_e32 v4, v4, v5
	v_add_f32_e32 v6, v6, v7
	v_add_f32_e32 v0, v0, v2
	v_add_f32_e32 v4, v4, v6
	v_add_f32_e32 v0, v0, v4
	v_mul_f32_e32 v0, 0x3be32166, v0
	v_mov_b32_e32 v1, 0
	global_store_dword v1, v0, s[0:1]
